# router weights interleaved by expert pair in LDS (no shuffle moves, same arithmetic); final LN gamma/beta loaded once before the row loop
# speedup vs baseline: 1.0126x; 1.0063x over previous
; #define LAS __attribute__((address_space(3)))
; DI KArgP kargs() { KArgP p = (KArgP)__builtin_amdgcn_kernarg_segment_ptr(); asm volatile("" : "+s"(p)); return p; }
; template <int l>
; DI void layer_body(LAS unsigned char* lds, const XcdBarrier& bar, const int lo, const int hi, const int G, const int vcu) {
;     ...
;             else { const float* wr = kargs()->in[13] + (size_t)(l / 2) * D_ * NE; LAS float* wT = (LAS float*)lds;
;                 for (int c = tid; c < D_; c += 512) { const f32x4 a = *(const f32x4*)(wr + (size_t)c * 8), b = *(const f32x4*)(wr + (size_t)c * 8 + 4);
;                     LAS float* wp = wT + ((c >> 2) & 1) * 1024 + ((c >> 9) * 64 + ((c >> 3) & 63)) * 4 + (c & 3);
;                     wp[0] = a[0]; wp[2048] = a[1]; wp[2 * 2048] = a[2]; wp[3 * 2048] = a[3]; wp[4 * 2048] = b[0]; wp[5 * 2048] = b[1]; wp[6 * 2048] = b[2]; wp[7 * 2048] = b[3]; }
.LBB0_1369:
	global_load_dwordx4 v[16:19], v[2:3], off offset:-16
	global_load_dwordx4 v[20:23], v[2:3], off
	v_lshl_add_u64 v[6:7], v[2:3], 0, s[16:17]
	global_load_dwordx4 v[24:27], v[6:7], off offset:-16
	global_load_dwordx4 v[28:31], v[6:7], off
	v_lshl_add_u64 v[6:7], v[6:7], 0, s[16:17]
	global_load_dwordx4 v[32:35], v[6:7], off offset:-16
	global_load_dwordx4 v[36:39], v[6:7], off
	v_lshl_add_u64 v[6:7], v[6:7], 0, s[16:17]
	global_load_dwordx4 v[40:43], v[6:7], off offset:-16
	global_load_dwordx4 v[44:47], v[6:7], off
	v_and_b32_e32 v12, 3, v0
	v_lshrrev_b32_e32 v13, 1, v12
	v_and_b32_e32 v12, 1, v12
	v_lshlrev_b32_e32 v13, 13, v13
	v_lshlrev_b32_e32 v12, 3, v12
	v_add_u32_e32 v14, v13, v12
	v_sub_u32_e32 v12, 12, v12
	v_add_u32_e32 v13, v13, v12
	v_and_b32_e32 v8, 0x400, v4
	v_lshlrev_b32_e32 v15, 1, v5
	v_lshlrev_b32_e32 v8, 2, v8
	v_and_b32_e32 v15, -16, v15
	v_add_u32_e32 v4, 0x20000, v4
	v_add_u32_e32 v5, 0x200, v5
	v_add_u32_e32 v15, v8, v15
	v_add_u32_e32 v8, v15, v14
	v_add_u32_e32 v48, v15, v13
	s_waitcnt vmcnt(7)
	ds_write2st64_b32 v48, v16, v19 offset1:64
	ds_write2st64_b32 v8, v17, v18 offset1:64
	s_waitcnt vmcnt(6)
	ds_write2st64_b32 v8, v20, v22 offset0:128 offset1:192
	ds_write2st64_b32 v48, v21, v23 offset0:128 offset1:192
	v_and_b32_e32 v9, 0x400, v4
	v_lshlrev_b32_e32 v15, 1, v5
	v_lshlrev_b32_e32 v9, 2, v9
	v_and_b32_e32 v15, -16, v15
	v_add_u32_e32 v4, 0x20000, v4
	v_add_u32_e32 v5, 0x200, v5
	v_add_u32_e32 v15, v9, v15
	v_add_u32_e32 v9, v15, v14
	v_add_u32_e32 v49, v15, v13
	s_waitcnt vmcnt(5)
	ds_write2st64_b32 v49, v24, v27 offset1:64
	ds_write2st64_b32 v9, v25, v26 offset1:64
	s_waitcnt vmcnt(4)
	ds_write2st64_b32 v9, v28, v30 offset0:128 offset1:192
	ds_write2st64_b32 v49, v29, v31 offset0:128 offset1:192
	v_and_b32_e32 v10, 0x400, v4
	v_lshlrev_b32_e32 v15, 1, v5
	v_lshlrev_b32_e32 v10, 2, v10
	v_and_b32_e32 v15, -16, v15
	v_add_u32_e32 v4, 0x20000, v4
	v_add_u32_e32 v5, 0x200, v5
	v_add_u32_e32 v15, v10, v15
	v_add_u32_e32 v10, v15, v14
	v_add_u32_e32 v50, v15, v13
	s_waitcnt vmcnt(3)
	ds_write2st64_b32 v50, v32, v35 offset1:64
	ds_write2st64_b32 v10, v33, v34 offset1:64
	s_waitcnt vmcnt(2)
	ds_write2st64_b32 v10, v36, v38 offset0:128 offset1:192
	ds_write2st64_b32 v50, v37, v39 offset0:128 offset1:192
	v_and_b32_e32 v11, 0x400, v4
	v_lshlrev_b32_e32 v15, 1, v5
	v_lshlrev_b32_e32 v11, 2, v11
	v_and_b32_e32 v15, -16, v15
	v_add_u32_e32 v4, 0x20000, v4
	v_add_u32_e32 v5, 0x200, v5
	v_add_u32_e32 v15, v11, v15
	v_add_u32_e32 v11, v15, v14
	v_add_u32_e32 v51, v15, v13
	s_waitcnt vmcnt(1)
	ds_write2st64_b32 v51, v40, v43 offset1:64
	ds_write2st64_b32 v11, v41, v42 offset1:64
	s_waitcnt vmcnt(0)
	ds_write2st64_b32 v11, v44, v46 offset0:128 offset1:192
	ds_write2st64_b32 v51, v45, v47 offset0:128 offset1:192

; #define LAS __attribute__((address_space(3)))
; template <bool ROUTE, bool COMBINE> ...
;     ...
;         for (int j = 0; j < 8; ++j) {
;             const f32x4 o = v[0]; const LAS float* wp = wT + (j & 1) * 1024 + ((j >> 1) * 64 + lane) * 4;
;             const f32x4 w0 = *(const LAS f32x4*)(wp), w1 = *(const LAS f32x4*)(wp + 2048), w2 = *(const LAS f32x4*)(wp + 2 * 2048), w3 = *(const LAS f32x4*)(wp + 3 * 2048);
;             const f32x4 w4 = *(const LAS f32x4*)(wp + 4 * 2048), w5 = *(const LAS f32x4*)(wp + 5 * 2048), w6 = *(const LAS f32x4*)(wp + 6 * 2048), w7 = *(const LAS f32x4*)(wp + 7 * 2048);
;             lg0 += (o[0] * w0[0] + o[1] * w0[1]) + (o[2] * w0[2] + o[3] * w0[3]); lg1 += (o[0] * w1[0] + o[1] * w1[1]) + (o[2] * w1[2] + o[3] * w1[3]);
;             lg2 += (o[0] * w2[0] + o[1] * w2[1]) + (o[2] * w2[2] + o[3] * w2[3]); lg3 += (o[0] * w3[0] + o[1] * w3[1]) + (o[2] * w3[2] + o[3] * w3[3]);
;             lg4 += (o[0] * w4[0] + o[1] * w4[1]) + (o[2] * w4[2] + o[3] * w4[3]); lg5 += (o[0] * w5[0] + o[1] * w5[1]) + (o[2] * w5[2] + o[3] * w5[3]);
;             lg6 += (o[0] * w6[0] + o[1] * w6[1]) + (o[2] * w6[2] + o[3] * w6[3]); lg7 += (o[0] * w7[0] + o[1] * w7[1]) + (o[2] * w7[2] + o[3] * w7[3]);
.LBB0_1378:
	s_and_b32 s8, s7, 0x400
	s_and_b32 s9, s6, 0xc0
	s_lshl_b32 s8, s8, 2
	v_or_b32_e32 v126, s9, v128
	s_add_i32 s8, s8, 0
	v_lshl_add_u32 v126, v126, 4, s8
	ds_read_b128 v[138:141], v126
	ds_read_b128 v[142:145], v126 offset:8192
	ds_read_b128 v[146:149], v126 offset:16384
	ds_read_b128 v[150:153], v126 offset:24576
	ds_read_b128 v[154:157], v126 offset:32768
	ds_read_b128 v[158:161], v126 offset:40960
	ds_read_b128 v[162:165], v126 offset:49152
	ds_read_b128 v[166:169], v126 offset:57344
	s_addk_i32 s7, 0x400
	s_add_i32 s6, s6, 32
	s_waitcnt lgkmcnt(6)
	v_pk_mul_f32 v[138:139], v[84:85], v[138:139]
	v_pk_mul_f32 v[142:143], v[82:83], v[142:143]
	v_pk_fma_f32 v[138:139], v[84:85], v[140:141], v[138:139] op_sel:[1,0,0] op_sel_hi:[0,1,1]
	v_pk_fma_f32 v[142:143], v[82:83], v[144:145], v[142:143] op_sel:[1,0,0] op_sel_hi:[0,1,1]
	s_waitcnt lgkmcnt(4)
	v_pk_mul_f32 v[146:147], v[84:85], v[146:147]
	v_pk_mul_f32 v[150:151], v[82:83], v[150:151]
	v_pk_fma_f32 v[146:147], v[84:85], v[148:149], v[146:147] op_sel:[1,0,0] op_sel_hi:[0,1,1]
	v_pk_fma_f32 v[150:151], v[82:83], v[152:153], v[150:151] op_sel:[1,0,0] op_sel_hi:[0,1,1]
	s_waitcnt lgkmcnt(2)
	v_pk_mul_f32 v[154:155], v[84:85], v[154:155]
	v_pk_mul_f32 v[158:159], v[82:83], v[158:159]
	v_pk_fma_f32 v[154:155], v[84:85], v[156:157], v[154:155] op_sel:[1,0,0] op_sel_hi:[0,1,1]
	v_pk_fma_f32 v[158:159], v[82:83], v[160:161], v[158:159] op_sel:[1,0,0] op_sel_hi:[0,1,1]
	s_waitcnt lgkmcnt(0)
	v_pk_mul_f32 v[162:163], v[84:85], v[162:163]
	v_pk_mul_f32 v[166:167], v[82:83], v[166:167]
	v_pk_fma_f32 v[162:163], v[84:85], v[164:165], v[162:163] op_sel:[1,0,0] op_sel_hi:[0,1,1]
	v_pk_fma_f32 v[166:167], v[82:83], v[168:169], v[166:167] op_sel:[1,0,0] op_sel_hi:[0,1,1]
	v_pk_add_f32 v[138:139], v[138:139], v[142:143]
	v_pk_add_f32 v[146:147], v[146:147], v[150:151]
	v_pk_add_f32 v[154:155], v[154:155], v[158:159]
	v_pk_add_f32 v[162:163], v[162:163], v[166:167]
	v_pk_add_f32 v[80:81], v[80:81], v[138:139]
	v_pk_add_f32 v[124:125], v[124:125], v[146:147]
	v_pk_add_f32 v[94:95], v[94:95], v[154:155]
	v_pk_add_f32 v[92:93], v[92:93], v[162:163]
	s_and_b32 s8, s7, 0x400
	s_and_b32 s9, s6, 0xc0
	s_lshl_b32 s8, s8, 2
	v_or_b32_e32 v126, s9, v128
	s_add_i32 s8, s8, 0
	v_lshl_add_u32 v126, v126, 4, s8
	ds_read_b128 v[138:141], v126
	ds_read_b128 v[142:145], v126 offset:8192
	ds_read_b128 v[146:149], v126 offset:16384
	ds_read_b128 v[150:153], v126 offset:24576
	ds_read_b128 v[154:157], v126 offset:32768
	ds_read_b128 v[158:161], v126 offset:40960
	ds_read_b128 v[162:165], v126 offset:49152
	ds_read_b128 v[166:169], v126 offset:57344
	s_addk_i32 s7, 0x400
	s_add_i32 s6, s6, 32
	s_waitcnt lgkmcnt(6)
	v_pk_mul_f32 v[138:139], v[88:89], v[138:139]
	v_pk_mul_f32 v[142:143], v[86:87], v[142:143]
	v_pk_fma_f32 v[138:139], v[88:89], v[140:141], v[138:139] op_sel:[1,0,0] op_sel_hi:[0,1,1]
	v_pk_fma_f32 v[142:143], v[86:87], v[144:145], v[142:143] op_sel:[1,0,0] op_sel_hi:[0,1,1]
	s_waitcnt lgkmcnt(4)
	v_pk_mul_f32 v[146:147], v[88:89], v[146:147]
	v_pk_mul_f32 v[150:151], v[86:87], v[150:151]
	v_pk_fma_f32 v[146:147], v[88:89], v[148:149], v[146:147] op_sel:[1,0,0] op_sel_hi:[0,1,1]
	v_pk_fma_f32 v[150:151], v[86:87], v[152:153], v[150:151] op_sel:[1,0,0] op_sel_hi:[0,1,1]
	s_waitcnt lgkmcnt(2)
	v_pk_mul_f32 v[154:155], v[88:89], v[154:155]
	v_pk_mul_f32 v[158:159], v[86:87], v[158:159]
	v_pk_fma_f32 v[154:155], v[88:89], v[156:157], v[154:155] op_sel:[1,0,0] op_sel_hi:[0,1,1]
	v_pk_fma_f32 v[158:159], v[86:87], v[160:161], v[158:159] op_sel:[1,0,0] op_sel_hi:[0,1,1]
	s_waitcnt lgkmcnt(0)
	v_pk_mul_f32 v[162:163], v[88:89], v[162:163]
	v_pk_mul_f32 v[166:167], v[86:87], v[166:167]
	v_pk_fma_f32 v[162:163], v[88:89], v[164:165], v[162:163] op_sel:[1,0,0] op_sel_hi:[0,1,1]
	v_pk_fma_f32 v[166:167], v[86:87], v[168:169], v[166:167] op_sel:[1,0,0] op_sel_hi:[0,1,1]
	v_pk_add_f32 v[138:139], v[138:139], v[142:143]
	v_pk_add_f32 v[146:147], v[146:147], v[150:151]
	v_pk_add_f32 v[154:155], v[154:155], v[158:159]
	v_pk_add_f32 v[162:163], v[162:163], v[166:167]
	v_pk_add_f32 v[80:81], v[80:81], v[138:139]
	v_pk_add_f32 v[124:125], v[124:125], v[146:147]
	v_pk_add_f32 v[94:95], v[94:95], v[154:155]
	v_pk_add_f32 v[92:93], v[92:93], v[162:163]
	s_and_b32 s8, s7, 0x400
	s_and_b32 s9, s6, 0xc0
	s_lshl_b32 s8, s8, 2
	v_or_b32_e32 v126, s9, v128
	s_add_i32 s8, s8, 0
	v_lshl_add_u32 v126, v126, 4, s8
	ds_read_b128 v[138:141], v126
	ds_read_b128 v[142:145], v126 offset:8192
	ds_read_b128 v[146:149], v126 offset:16384
	ds_read_b128 v[150:153], v126 offset:24576
	ds_read_b128 v[154:157], v126 offset:32768
	ds_read_b128 v[158:161], v126 offset:40960
	ds_read_b128 v[162:165], v126 offset:49152
	ds_read_b128 v[166:169], v126 offset:57344
	s_addk_i32 s7, 0x400
	s_add_i32 s6, s6, 32
	s_waitcnt lgkmcnt(6)
	v_pk_mul_f32 v[138:139], v[110:111], v[138:139]
	v_pk_mul_f32 v[142:143], v[90:91], v[142:143]
	v_pk_fma_f32 v[138:139], v[110:111], v[140:141], v[138:139] op_sel:[1,0,0] op_sel_hi:[0,1,1]
	v_pk_fma_f32 v[142:143], v[90:91], v[144:145], v[142:143] op_sel:[1,0,0] op_sel_hi:[0,1,1]
	s_waitcnt lgkmcnt(4)
	v_pk_mul_f32 v[146:147], v[110:111], v[146:147]
	v_pk_mul_f32 v[150:151], v[90:91], v[150:151]
	v_pk_fma_f32 v[146:147], v[110:111], v[148:149], v[146:147] op_sel:[1,0,0] op_sel_hi:[0,1,1]
	v_pk_fma_f32 v[150:151], v[90:91], v[152:153], v[150:151] op_sel:[1,0,0] op_sel_hi:[0,1,1]
	s_waitcnt lgkmcnt(2)
	v_pk_mul_f32 v[154:155], v[110:111], v[154:155]
	v_pk_mul_f32 v[158:159], v[90:91], v[158:159]
	v_pk_fma_f32 v[154:155], v[110:111], v[156:157], v[154:155] op_sel:[1,0,0] op_sel_hi:[0,1,1]
	v_pk_fma_f32 v[158:159], v[90:91], v[160:161], v[158:159] op_sel:[1,0,0] op_sel_hi:[0,1,1]
	s_waitcnt lgkmcnt(0)
; #define LAS __attribute__((address_space(3)))
; template <bool ROUTE, bool COMBINE> ...
;     ...
;         for (int j = 0; j < 8; ++j) {
;             const f32x4 o = v[0]; const LAS float* wp = wT + (j & 1) * 1024 + ((j >> 1) * 64 + lane) * 4;
;             const f32x4 w0 = *(const LAS f32x4*)(wp), w1 = *(const LAS f32x4*)(wp + 2048), w2 = *(const LAS f32x4*)(wp + 2 * 2048), w3 = *(const LAS f32x4*)(wp + 3 * 2048);
;             const f32x4 w4 = *(const LAS f32x4*)(wp + 4 * 2048), w5 = *(const LAS f32x4*)(wp + 5 * 2048), w6 = *(const LAS f32x4*)(wp + 6 * 2048), w7 = *(const LAS f32x4*)(wp + 7 * 2048);
;             lg0 += (o[0] * w0[0] + o[1] * w0[1]) + (o[2] * w0[2] + o[3] * w0[3]); lg1 += (o[0] * w1[0] + o[1] * w1[1]) + (o[2] * w1[2] + o[3] * w1[3]);
;             lg2 += (o[0] * w2[0] + o[1] * w2[1]) + (o[2] * w2[2] + o[3] * w2[3]); lg3 += (o[0] * w3[0] + o[1] * w3[1]) + (o[2] * w3[2] + o[3] * w3[3]);
;             lg4 += (o[0] * w4[0] + o[1] * w4[1]) + (o[2] * w4[2] + o[3] * w4[3]); lg5 += (o[0] * w5[0] + o[1] * w5[1]) + (o[2] * w5[2] + o[3] * w5[3]);
;             lg6 += (o[0] * w6[0] + o[1] * w6[1]) + (o[2] * w6[2] + o[3] * w6[3]); lg7 += (o[0] * w7[0] + o[1] * w7[1]) + (o[2] * w7[2] + o[3] * w7[3]);
; #pragma unroll
;             for (int jj = 0; jj < 7; ++jj) v[jj] = v[jj + 1];
;         }
	v_pk_mul_f32 v[162:163], v[110:111], v[162:163]
	v_pk_mul_f32 v[166:167], v[90:91], v[166:167]
	v_pk_fma_f32 v[162:163], v[110:111], v[164:165], v[162:163] op_sel:[1,0,0] op_sel_hi:[0,1,1]
	v_pk_fma_f32 v[166:167], v[90:91], v[168:169], v[166:167] op_sel:[1,0,0] op_sel_hi:[0,1,1]
	v_pk_add_f32 v[138:139], v[138:139], v[142:143]
	v_pk_add_f32 v[146:147], v[146:147], v[150:151]
	v_pk_add_f32 v[154:155], v[154:155], v[158:159]
	v_pk_add_f32 v[162:163], v[162:163], v[166:167]
	v_pk_add_f32 v[80:81], v[80:81], v[138:139]
	v_pk_add_f32 v[124:125], v[124:125], v[146:147]
	v_pk_add_f32 v[94:95], v[94:95], v[154:155]
	v_pk_add_f32 v[92:93], v[92:93], v[162:163]
	s_and_b32 s8, s7, 0x400
	s_and_b32 s9, s6, 0xc0
	s_lshl_b32 s8, s8, 2
	v_or_b32_e32 v126, s9, v128
	s_add_i32 s8, s8, 0
	v_lshl_add_u32 v126, v126, 4, s8
	ds_read_b128 v[138:141], v126
	ds_read_b128 v[142:145], v126 offset:8192
	ds_read_b128 v[146:149], v126 offset:16384
	ds_read_b128 v[150:153], v126 offset:24576
	ds_read_b128 v[154:157], v126 offset:32768
	ds_read_b128 v[158:161], v126 offset:40960
	ds_read_b128 v[162:165], v126 offset:49152
	ds_read_b128 v[166:169], v126 offset:57344
	s_addk_i32 s7, 0x400
	s_add_i32 s6, s6, 32
	s_waitcnt lgkmcnt(6)
	v_pk_mul_f32 v[138:139], v[114:115], v[138:139]
	v_pk_mul_f32 v[142:143], v[112:113], v[142:143]
	v_pk_fma_f32 v[138:139], v[114:115], v[140:141], v[138:139] op_sel:[1,0,0] op_sel_hi:[0,1,1]
	v_pk_fma_f32 v[142:143], v[112:113], v[144:145], v[142:143] op_sel:[1,0,0] op_sel_hi:[0,1,1]
	s_waitcnt lgkmcnt(4)
	v_pk_mul_f32 v[146:147], v[114:115], v[146:147]
	v_pk_mul_f32 v[150:151], v[112:113], v[150:151]
	v_pk_fma_f32 v[146:147], v[114:115], v[148:149], v[146:147] op_sel:[1,0,0] op_sel_hi:[0,1,1]
	v_pk_fma_f32 v[150:151], v[112:113], v[152:153], v[150:151] op_sel:[1,0,0] op_sel_hi:[0,1,1]
	s_waitcnt lgkmcnt(2)
	v_pk_mul_f32 v[154:155], v[114:115], v[154:155]
	v_pk_mul_f32 v[158:159], v[112:113], v[158:159]
	v_pk_fma_f32 v[154:155], v[114:115], v[156:157], v[154:155] op_sel:[1,0,0] op_sel_hi:[0,1,1]
	v_pk_fma_f32 v[158:159], v[112:113], v[160:161], v[158:159] op_sel:[1,0,0] op_sel_hi:[0,1,1]
	s_waitcnt lgkmcnt(0)
	v_pk_mul_f32 v[162:163], v[114:115], v[162:163]
	v_pk_mul_f32 v[166:167], v[112:113], v[166:167]
	v_pk_fma_f32 v[162:163], v[114:115], v[164:165], v[162:163] op_sel:[1,0,0] op_sel_hi:[0,1,1]
	v_pk_fma_f32 v[166:167], v[112:113], v[168:169], v[166:167] op_sel:[1,0,0] op_sel_hi:[0,1,1]
	v_pk_add_f32 v[138:139], v[138:139], v[142:143]
	v_pk_add_f32 v[146:147], v[146:147], v[150:151]
	v_pk_add_f32 v[154:155], v[154:155], v[158:159]
	v_pk_add_f32 v[162:163], v[162:163], v[166:167]
	v_pk_add_f32 v[80:81], v[80:81], v[138:139]
	v_pk_add_f32 v[124:125], v[124:125], v[146:147]
	v_pk_add_f32 v[94:95], v[94:95], v[154:155]
	v_pk_add_f32 v[92:93], v[92:93], v[162:163]
	s_and_b32 s8, s7, 0x400
	s_and_b32 s9, s6, 0xc0
	s_lshl_b32 s8, s8, 2
	v_or_b32_e32 v126, s9, v128
	s_add_i32 s8, s8, 0
	v_lshl_add_u32 v126, v126, 4, s8
	ds_read_b128 v[138:141], v126
	ds_read_b128 v[142:145], v126 offset:8192
	ds_read_b128 v[146:149], v126 offset:16384
	ds_read_b128 v[150:153], v126 offset:24576
	ds_read_b128 v[154:157], v126 offset:32768
	ds_read_b128 v[158:161], v126 offset:40960
	ds_read_b128 v[162:165], v126 offset:49152
	ds_read_b128 v[166:169], v126 offset:57344
	s_addk_i32 s7, 0x400
	s_add_i32 s6, s6, 32
	s_waitcnt lgkmcnt(6)
	v_pk_mul_f32 v[138:139], v[118:119], v[138:139]
	v_pk_mul_f32 v[142:143], v[116:117], v[142:143]
	v_pk_fma_f32 v[138:139], v[118:119], v[140:141], v[138:139] op_sel:[1,0,0] op_sel_hi:[0,1,1]
	v_pk_fma_f32 v[142:143], v[116:117], v[144:145], v[142:143] op_sel:[1,0,0] op_sel_hi:[0,1,1]
	s_waitcnt lgkmcnt(4)
	v_pk_mul_f32 v[146:147], v[118:119], v[146:147]
	v_pk_mul_f32 v[150:151], v[116:117], v[150:151]
	v_pk_fma_f32 v[146:147], v[118:119], v[148:149], v[146:147] op_sel:[1,0,0] op_sel_hi:[0,1,1]
	v_pk_fma_f32 v[150:151], v[116:117], v[152:153], v[150:151] op_sel:[1,0,0] op_sel_hi:[0,1,1]
	s_waitcnt lgkmcnt(2)
	v_pk_mul_f32 v[154:155], v[118:119], v[154:155]
	v_pk_mul_f32 v[158:159], v[116:117], v[158:159]
	v_pk_fma_f32 v[154:155], v[118:119], v[156:157], v[154:155] op_sel:[1,0,0] op_sel_hi:[0,1,1]
	v_pk_fma_f32 v[158:159], v[116:117], v[160:161], v[158:159] op_sel:[1,0,0] op_sel_hi:[0,1,1]
	s_waitcnt lgkmcnt(0)
	v_pk_mul_f32 v[162:163], v[118:119], v[162:163]
	v_pk_mul_f32 v[166:167], v[116:117], v[166:167]
	v_pk_fma_f32 v[162:163], v[118:119], v[164:165], v[162:163] op_sel:[1,0,0] op_sel_hi:[0,1,1]
	v_pk_fma_f32 v[166:167], v[116:117], v[168:169], v[166:167] op_sel:[1,0,0] op_sel_hi:[0,1,1]
	v_pk_add_f32 v[138:139], v[138:139], v[142:143]
	v_pk_add_f32 v[146:147], v[146:147], v[150:151]
	v_pk_add_f32 v[154:155], v[154:155], v[158:159]
	v_pk_add_f32 v[162:163], v[162:163], v[166:167]
	v_pk_add_f32 v[80:81], v[80:81], v[138:139]
	v_pk_add_f32 v[124:125], v[124:125], v[146:147]
	v_pk_add_f32 v[94:95], v[94:95], v[154:155]
	v_pk_add_f32 v[92:93], v[92:93], v[162:163]
	s_and_b32 s8, s7, 0x400
	s_and_b32 s9, s6, 0xc0
	s_lshl_b32 s8, s8, 2
	v_or_b32_e32 v126, s9, v128
	s_add_i32 s8, s8, 0
	v_lshl_add_u32 v126, v126, 4, s8
	ds_read_b128 v[138:141], v126
	ds_read_b128 v[142:145], v126 offset:8192
	ds_read_b128 v[146:149], v126 offset:16384
	ds_read_b128 v[150:153], v126 offset:24576
	ds_read_b128 v[154:157], v126 offset:32768
	ds_read_b128 v[158:161], v126 offset:40960
	ds_read_b128 v[162:165], v126 offset:49152
	ds_read_b128 v[166:169], v126 offset:57344
	s_addk_i32 s7, 0x400
	s_add_i32 s6, s6, 32
	s_waitcnt lgkmcnt(6)
; #define LAS __attribute__((address_space(3)))
; template <bool ROUTE, bool COMBINE> ...
;     ...
;         for (int j = 0; j < 8; ++j) {
;             const f32x4 o = v[0]; const LAS float* wp = wT + (j & 1) * 1024 + ((j >> 1) * 64 + lane) * 4;
;             const f32x4 w0 = *(const LAS f32x4*)(wp), w1 = *(const LAS f32x4*)(wp + 2048), w2 = *(const LAS f32x4*)(wp + 2 * 2048), w3 = *(const LAS f32x4*)(wp + 3 * 2048);
;             const f32x4 w4 = *(const LAS f32x4*)(wp + 4 * 2048), w5 = *(const LAS f32x4*)(wp + 5 * 2048), w6 = *(const LAS f32x4*)(wp + 6 * 2048), w7 = *(const LAS f32x4*)(wp + 7 * 2048);
;             lg0 += (o[0] * w0[0] + o[1] * w0[1]) + (o[2] * w0[2] + o[3] * w0[3]); lg1 += (o[0] * w1[0] + o[1] * w1[1]) + (o[2] * w1[2] + o[3] * w1[3]);
;             lg2 += (o[0] * w2[0] + o[1] * w2[1]) + (o[2] * w2[2] + o[3] * w2[3]); lg3 += (o[0] * w3[0] + o[1] * w3[1]) + (o[2] * w3[2] + o[3] * w3[3]);
;             lg4 += (o[0] * w4[0] + o[1] * w4[1]) + (o[2] * w4[2] + o[3] * w4[3]); lg5 += (o[0] * w5[0] + o[1] * w5[1]) + (o[2] * w5[2] + o[3] * w5[3]);
;             lg6 += (o[0] * w6[0] + o[1] * w6[1]) + (o[2] * w6[2] + o[3] * w6[3]); lg7 += (o[0] * w7[0] + o[1] * w7[1]) + (o[2] * w7[2] + o[3] * w7[3]);
; #pragma unroll
;             for (int jj = 0; jj < 7; ++jj) v[jj] = v[jj + 1];
;         }
	v_pk_mul_f32 v[138:139], v[122:123], v[138:139]
	v_pk_mul_f32 v[142:143], v[120:121], v[142:143]
	v_pk_fma_f32 v[138:139], v[122:123], v[140:141], v[138:139] op_sel:[1,0,0] op_sel_hi:[0,1,1]
	v_pk_fma_f32 v[142:143], v[120:121], v[144:145], v[142:143] op_sel:[1,0,0] op_sel_hi:[0,1,1]
	s_waitcnt lgkmcnt(4)
	v_pk_mul_f32 v[146:147], v[122:123], v[146:147]
	v_pk_mul_f32 v[150:151], v[120:121], v[150:151]
	v_pk_fma_f32 v[146:147], v[122:123], v[148:149], v[146:147] op_sel:[1,0,0] op_sel_hi:[0,1,1]
	v_pk_fma_f32 v[150:151], v[120:121], v[152:153], v[150:151] op_sel:[1,0,0] op_sel_hi:[0,1,1]
	s_waitcnt lgkmcnt(2)
	v_pk_mul_f32 v[154:155], v[122:123], v[154:155]
	v_pk_mul_f32 v[158:159], v[120:121], v[158:159]
	v_pk_fma_f32 v[154:155], v[122:123], v[156:157], v[154:155] op_sel:[1,0,0] op_sel_hi:[0,1,1]
	v_pk_fma_f32 v[158:159], v[120:121], v[160:161], v[158:159] op_sel:[1,0,0] op_sel_hi:[0,1,1]
	s_waitcnt lgkmcnt(0)
	v_pk_mul_f32 v[162:163], v[122:123], v[162:163]
	v_pk_mul_f32 v[166:167], v[120:121], v[166:167]
	v_pk_fma_f32 v[162:163], v[122:123], v[164:165], v[162:163] op_sel:[1,0,0] op_sel_hi:[0,1,1]
	v_pk_fma_f32 v[166:167], v[120:121], v[168:169], v[166:167] op_sel:[1,0,0] op_sel_hi:[0,1,1]
	v_pk_add_f32 v[138:139], v[138:139], v[142:143]
	v_pk_add_f32 v[146:147], v[146:147], v[150:151]
	v_pk_add_f32 v[154:155], v[154:155], v[158:159]
	v_pk_add_f32 v[162:163], v[162:163], v[166:167]
	v_pk_add_f32 v[80:81], v[80:81], v[138:139]
	v_pk_add_f32 v[124:125], v[124:125], v[146:147]
	v_pk_add_f32 v[94:95], v[94:95], v[154:155]
	v_pk_add_f32 v[92:93], v[92:93], v[162:163]
	s_and_b32 s8, s7, 0x400
	s_and_b32 s9, s6, 0xc0
	s_lshl_b32 s8, s8, 2
	v_or_b32_e32 v126, s9, v128
	s_add_i32 s8, s8, 0
	v_lshl_add_u32 v126, v126, 4, s8
	ds_read_b128 v[138:141], v126
	ds_read_b128 v[142:145], v126 offset:8192
	ds_read_b128 v[146:149], v126 offset:16384
	ds_read_b128 v[150:153], v126 offset:24576
	ds_read_b128 v[154:157], v126 offset:32768
	ds_read_b128 v[158:161], v126 offset:40960
	ds_read_b128 v[162:165], v126 offset:49152
	ds_read_b128 v[166:169], v126 offset:57344
	s_addk_i32 s7, 0x400
	s_add_i32 s6, s6, 32
	s_waitcnt lgkmcnt(6)
	v_pk_mul_f32 v[138:139], v[108:109], v[138:139]
	v_pk_mul_f32 v[142:143], v[106:107], v[142:143]
	v_pk_fma_f32 v[138:139], v[108:109], v[140:141], v[138:139] op_sel:[1,0,0] op_sel_hi:[0,1,1]
	v_pk_fma_f32 v[142:143], v[106:107], v[144:145], v[142:143] op_sel:[1,0,0] op_sel_hi:[0,1,1]
	s_waitcnt lgkmcnt(4)
	v_pk_mul_f32 v[146:147], v[108:109], v[146:147]
	v_pk_mul_f32 v[150:151], v[106:107], v[150:151]
	v_pk_fma_f32 v[146:147], v[108:109], v[148:149], v[146:147] op_sel:[1,0,0] op_sel_hi:[0,1,1]
	v_pk_fma_f32 v[150:151], v[106:107], v[152:153], v[150:151] op_sel:[1,0,0] op_sel_hi:[0,1,1]
	s_waitcnt lgkmcnt(2)
	v_pk_mul_f32 v[154:155], v[108:109], v[154:155]
	v_pk_mul_f32 v[158:159], v[106:107], v[158:159]
	v_pk_fma_f32 v[154:155], v[108:109], v[156:157], v[154:155] op_sel:[1,0,0] op_sel_hi:[0,1,1]
	v_pk_fma_f32 v[158:159], v[106:107], v[160:161], v[158:159] op_sel:[1,0,0] op_sel_hi:[0,1,1]
	s_waitcnt lgkmcnt(0)
	v_pk_mul_f32 v[162:163], v[108:109], v[162:163]
	v_pk_mul_f32 v[166:167], v[106:107], v[166:167]
	v_pk_fma_f32 v[162:163], v[108:109], v[164:165], v[162:163] op_sel:[1,0,0] op_sel_hi:[0,1,1]
	v_pk_fma_f32 v[166:167], v[106:107], v[168:169], v[166:167] op_sel:[1,0,0] op_sel_hi:[0,1,1]
	v_pk_add_f32 v[138:139], v[138:139], v[142:143]
	v_pk_add_f32 v[146:147], v[146:147], v[150:151]
	v_pk_add_f32 v[154:155], v[154:155], v[158:159]
	v_pk_add_f32 v[162:163], v[162:163], v[166:167]
	v_pk_add_f32 v[80:81], v[80:81], v[138:139]
	v_pk_add_f32 v[124:125], v[124:125], v[146:147]
	v_pk_add_f32 v[94:95], v[94:95], v[154:155]
	v_pk_add_f32 v[92:93], v[92:93], v[162:163]
	s_and_b32 s8, s7, 0x400
	s_and_b32 s9, s6, 0xc0
	s_lshl_b32 s8, s8, 2
	v_or_b32_e32 v126, s9, v128
	s_add_i32 s8, s8, 0
	v_lshl_add_u32 v126, v126, 4, s8
	ds_read_b128 v[138:141], v126
	ds_read_b128 v[142:145], v126 offset:8192
	ds_read_b128 v[146:149], v126 offset:16384
	ds_read_b128 v[150:153], v126 offset:24576
	ds_read_b128 v[154:157], v126 offset:32768
	ds_read_b128 v[158:161], v126 offset:40960
	ds_read_b128 v[162:165], v126 offset:49152
	ds_read_b128 v[166:169], v126 offset:57344
	s_addk_i32 s7, 0x400
	s_add_i32 s6, s6, 32
	s_waitcnt lgkmcnt(6)
	v_pk_mul_f32 v[138:139], v[104:105], v[138:139]
	v_pk_mul_f32 v[142:143], v[102:103], v[142:143]
	v_pk_fma_f32 v[138:139], v[104:105], v[140:141], v[138:139] op_sel:[1,0,0] op_sel_hi:[0,1,1]
	v_pk_fma_f32 v[142:143], v[102:103], v[144:145], v[142:143] op_sel:[1,0,0] op_sel_hi:[0,1,1]
	s_waitcnt lgkmcnt(4)
	v_pk_mul_f32 v[146:147], v[104:105], v[146:147]
	v_pk_mul_f32 v[150:151], v[102:103], v[150:151]
	v_pk_fma_f32 v[146:147], v[104:105], v[148:149], v[146:147] op_sel:[1,0,0] op_sel_hi:[0,1,1]
	v_pk_fma_f32 v[150:151], v[102:103], v[152:153], v[150:151] op_sel:[1,0,0] op_sel_hi:[0,1,1]
	s_waitcnt lgkmcnt(2)
	v_pk_mul_f32 v[154:155], v[104:105], v[154:155]
	v_pk_mul_f32 v[158:159], v[102:103], v[158:159]
	v_pk_fma_f32 v[154:155], v[104:105], v[156:157], v[154:155] op_sel:[1,0,0] op_sel_hi:[0,1,1]
	v_pk_fma_f32 v[158:159], v[102:103], v[160:161], v[158:159] op_sel:[1,0,0] op_sel_hi:[0,1,1]
	s_waitcnt lgkmcnt(0)
; #define LAS __attribute__((address_space(3)))
; template <bool ROUTE, bool COMBINE> ...
;     ...
;         for (int j = 0; j < 8; ++j) {
;             const f32x4 o = v[0]; const LAS float* wp = wT + (j & 1) * 1024 + ((j >> 1) * 64 + lane) * 4;
;             const f32x4 w0 = *(const LAS f32x4*)(wp), w1 = *(const LAS f32x4*)(wp + 2048), w2 = *(const LAS f32x4*)(wp + 2 * 2048), w3 = *(const LAS f32x4*)(wp + 3 * 2048);
;             const f32x4 w4 = *(const LAS f32x4*)(wp + 4 * 2048), w5 = *(const LAS f32x4*)(wp + 5 * 2048), w6 = *(const LAS f32x4*)(wp + 6 * 2048), w7 = *(const LAS f32x4*)(wp + 7 * 2048);
;             lg0 += (o[0] * w0[0] + o[1] * w0[1]) + (o[2] * w0[2] + o[3] * w0[3]); lg1 += (o[0] * w1[0] + o[1] * w1[1]) + (o[2] * w1[2] + o[3] * w1[3]);
;             lg2 += (o[0] * w2[0] + o[1] * w2[1]) + (o[2] * w2[2] + o[3] * w2[3]); lg3 += (o[0] * w3[0] + o[1] * w3[1]) + (o[2] * w3[2] + o[3] * w3[3]);
;             lg4 += (o[0] * w4[0] + o[1] * w4[1]) + (o[2] * w4[2] + o[3] * w4[3]); lg5 += (o[0] * w5[0] + o[1] * w5[1]) + (o[2] * w5[2] + o[3] * w5[3]);
;             lg6 += (o[0] * w6[0] + o[1] * w6[1]) + (o[2] * w6[2] + o[3] * w6[3]); lg7 += (o[0] * w7[0] + o[1] * w7[1]) + (o[2] * w7[2] + o[3] * w7[3]);
; #pragma unroll
;             for (int jj = 0; jj < 7; ++jj) v[jj] = v[jj + 1];
;         }
;         float lg[8] = {wave_sum(lg0), wave_sum(lg1), wave_sum(lg2), wave_sum(lg3), wave_sum(lg4), wave_sum(lg5), wave_sum(lg6), wave_sum(lg7)};
;         if (lane == 0) {
;             int i0 = 0; float v0 = lg[0];
; #pragma unroll
;             for (int e = 1; e < 8; ++e) if (lg[e] > v0) { v0 = lg[e]; i0 = e; }
;             int i1 = -1; float v1 = -3.0e38f;
; #pragma unroll
;             for (int e = 0; e < 8; ++e) if (e != i0 && lg[e] > v1) { v1 = lg[e]; i1 = e; }
;             const float e1 = expf(v1 - v0), g0 = 1.0f / (1.0f + e1), g1 = e1 / (1.0f + e1);
;             tope[row * 2] = i0; tope[row * 2 + 1] = i1; topg[row * 2] = g0; topg[row * 2 + 1] = g1;
	v_pk_mul_f32 v[162:163], v[104:105], v[162:163]
	v_pk_mul_f32 v[166:167], v[102:103], v[166:167]
	v_pk_fma_f32 v[162:163], v[104:105], v[164:165], v[162:163] op_sel:[1,0,0] op_sel_hi:[0,1,1]
	v_pk_fma_f32 v[166:167], v[102:103], v[168:169], v[166:167] op_sel:[1,0,0] op_sel_hi:[0,1,1]
	v_pk_add_f32 v[138:139], v[138:139], v[142:143]
	v_pk_add_f32 v[146:147], v[146:147], v[150:151]
	v_pk_add_f32 v[154:155], v[154:155], v[158:159]
	v_pk_add_f32 v[162:163], v[162:163], v[166:167]
	v_pk_add_f32 v[80:81], v[80:81], v[138:139]
	v_pk_add_f32 v[124:125], v[124:125], v[146:147]
	v_pk_add_f32 v[94:95], v[94:95], v[154:155]
	v_pk_add_f32 v[92:93], v[92:93], v[162:163]
	ds_bpermute_b32 v83, v129, v81
	ds_bpermute_b32 v82, v129, v80
	ds_bpermute_b32 v84, v129, v124
	ds_bpermute_b32 v85, v129, v125
	ds_bpermute_b32 v86, v129, v94
	ds_bpermute_b32 v91, v129, v95
	s_waitcnt lgkmcnt(4)
	v_pk_add_f32 v[80:81], v[80:81], v[82:83]
	ds_bpermute_b32 v83, v130, v81
	ds_bpermute_b32 v82, v130, v80
	s_waitcnt lgkmcnt(5)
	v_add_f32_e32 v84, v124, v84
	ds_bpermute_b32 v87, v130, v84
	s_waitcnt lgkmcnt(5)
	v_add_f32_e32 v85, v125, v85
	s_waitcnt lgkmcnt(4)
	v_add_f32_e32 v86, v94, v86
	s_waitcnt lgkmcnt(1)
	v_pk_add_f32 v[80:81], v[80:81], v[82:83]
	ds_bpermute_b32 v83, v131, v81
	ds_bpermute_b32 v82, v131, v80
	s_waitcnt lgkmcnt(2)
	v_add_f32_e32 v84, v84, v87
	ds_bpermute_b32 v88, v130, v85
	ds_bpermute_b32 v89, v130, v86
	ds_bpermute_b32 v87, v131, v84
	s_waitcnt lgkmcnt(3)
	v_pk_add_f32 v[80:81], v[80:81], v[82:83]
	ds_bpermute_b32 v83, v132, v81
	ds_bpermute_b32 v82, v132, v80
	s_waitcnt lgkmcnt(4)
	v_add_f32_e32 v85, v85, v88
	s_waitcnt lgkmcnt(2)
	v_add_f32_e32 v84, v84, v87
	ds_bpermute_b32 v88, v131, v85
	ds_bpermute_b32 v87, v132, v84
	s_waitcnt lgkmcnt(2)
	v_pk_add_f32 v[80:81], v[80:81], v[82:83]
	ds_bpermute_b32 v83, v133, v81
	ds_bpermute_b32 v82, v133, v80
	s_waitcnt lgkmcnt(3)
	v_add_f32_e32 v85, v85, v88
	s_waitcnt lgkmcnt(2)
	v_add_f32_e32 v84, v84, v87
	ds_bpermute_b32 v87, v132, v85
	ds_bpermute_b32 v88, v133, v84
	s_waitcnt lgkmcnt(2)
	v_pk_add_f32 v[80:81], v[80:81], v[82:83]
	v_add_f32_e32 v82, v86, v89
	ds_bpermute_b32 v86, v131, v82
	s_waitcnt lgkmcnt(2)
	v_add_f32_e32 v87, v85, v87
	s_waitcnt lgkmcnt(1)
	v_add_f32_e32 v85, v84, v88
	ds_bpermute_b32 v94, v129, v93
	v_add_f32_e32 v91, v95, v91
	s_waitcnt lgkmcnt(1)
	v_add_f32_e32 v86, v82, v86
	ds_bpermute_b32 v89, v132, v86
	ds_bpermute_b32 v95, v130, v91
	s_waitcnt lgkmcnt(2)
	v_add_f32_e32 v93, v93, v94
	ds_bpermute_b32 v94, v130, v93
	ds_bpermute_b32 v90, v133, v87
	s_waitcnt lgkmcnt(3)
	v_add_f32_e32 v84, v86, v89
	ds_bpermute_b32 v89, v133, v84
	s_waitcnt lgkmcnt(3)
	v_add_f32_e32 v91, v91, v95
	s_waitcnt lgkmcnt(2)
	v_add_f32_e32 v93, v93, v94
	ds_bpermute_b32 v95, v131, v91
	ds_bpermute_b32 v94, v131, v93
	s_waitcnt lgkmcnt(2)
	v_add_f32_e32 v89, v84, v89
	ds_bpermute_b32 v84, v129, v92
	v_add_f32_e32 v87, v87, v90
	s_waitcnt lgkmcnt(2)
	v_add_f32_e32 v91, v91, v95
	s_waitcnt lgkmcnt(1)
	v_add_f32_e32 v93, v93, v94
	ds_bpermute_b32 v95, v132, v91
	s_waitcnt lgkmcnt(1)
	v_add_f32_e32 v84, v92, v84
	ds_bpermute_b32 v92, v130, v84
	ds_bpermute_b32 v94, v132, v93
	ds_bpermute_b32 v83, v134, v81
	s_waitcnt lgkmcnt(3)
	v_add_f32_e32 v91, v91, v95
	ds_bpermute_b32 v95, v133, v91
	s_waitcnt lgkmcnt(3)
	v_add_f32_e32 v84, v84, v92
	ds_bpermute_b32 v92, v131, v84
	s_waitcnt lgkmcnt(3)
	v_add_f32_e32 v103, v93, v94
	ds_bpermute_b32 v104, v133, v103
	s_waitcnt lgkmcnt(2)
	v_add_f32_e32 v91, v91, v95
	ds_bpermute_b32 v82, v134, v80
	s_waitcnt lgkmcnt(2)
	v_add_f32_e32 v84, v84, v92
	ds_bpermute_b32 v92, v132, v84
	ds_bpermute_b32 v86, v134, v85
	ds_bpermute_b32 v88, v134, v87
	ds_bpermute_b32 v90, v134, v89
	s_waitcnt lgkmcnt(3)
	v_add_f32_e32 v84, v84, v92
	ds_bpermute_b32 v102, v133, v84
	ds_bpermute_b32 v92, v134, v91
	s_waitcnt lgkmcnt(1)
	v_add_f32_e32 v93, v84, v102
	v_add_f32_e32 v84, v103, v104
	ds_bpermute_b32 v94, v134, v93
	ds_bpermute_b32 v95, v134, v84
	s_and_saveexec_b64 s[22:23], s[4:5]
	s_cbranch_execz .LBB0_1374
	v_add_f32_e32 v88, v87, v88
	v_add_f32_e32 v85, v85, v86
	v_pk_add_f32 v[86:87], v[80:81], v[82:83]
	v_add_f32_e32 v89, v89, v90
	v_cmp_gt_f32_e32 vcc, v86, v87
	s_waitcnt lgkmcnt(2)
	v_add_f32_e32 v91, v91, v92
	s_waitcnt lgkmcnt(1)
	v_add_f32_e32 v93, v93, v94
	v_cndmask_b32_e32 v81, v87, v86, vcc
	v_cndmask_b32_e64 v80, 0, 1, vcc
	v_cmp_gt_f32_e32 vcc, v85, v81
	s_waitcnt lgkmcnt(0)
	v_add_f32_e32 v84, v84, v95
	v_cmp_nlt_f32_e64 s[12:13], s35, v87
	v_cndmask_b32_e32 v81, v81, v85, vcc
	v_cndmask_b32_e64 v80, v80, 2, vcc
	v_cmp_gt_f32_e32 vcc, v88, v81
	s_nop 1
	v_cndmask_b32_e32 v81, v81, v88, vcc
	v_cndmask_b32_e64 v80, v80, 3, vcc
	v_cmp_gt_f32_e32 vcc, v89, v81
	s_nop 1
	v_cndmask_b32_e32 v81, v81, v89, vcc
	v_cndmask_b32_e64 v80, v80, 4, vcc
	v_cmp_gt_f32_e32 vcc, v91, v81
	s_nop 1
	v_cndmask_b32_e32 v81, v81, v91, vcc
	v_cndmask_b32_e64 v80, v80, 5, vcc
	v_cmp_ngt_f32_e32 vcc, v93, v81
	s_nop 1
	v_cndmask_b32_e32 v82, v93, v81, vcc
	v_cndmask_b32_e32 v80, 6, v80, vcc
	v_cmp_gt_f32_e64 s[8:9], v84, v82
	v_cmp_ngt_f32_e64 s[6:7], v84, v82
	s_nop 0
	v_cndmask_b32_e64 v80, v80, 7, s[8:9]
	v_cmp_eq_u32_e64 s[10:11], 0, v80
	s_or_b64 s[10:11], s[10:11], s[12:13]
	s_or_b64 s[8:9], vcc, s[8:9]
	v_cndmask_b32_e64 v83, v87, v136, s[10:11]
	v_cndmask_b32_e64 v81, 0, -1, s[10:11]
	v_cmp_ne_u32_e64 s[10:11], 1, v80
	v_cmp_gt_f32_e64 s[12:13], v86, v83
	s_and_b64 s[10:11], s[10:11], s[12:13]
	v_cndmask_b32_e64 v83, v83, v86, s[10:11]
	v_cndmask_b32_e64 v81, v81, 1, s[10:11]
	v_cmp_ne_u32_e64 s[10:11], 2, v80
	v_cmp_gt_f32_e64 s[12:13], v85, v83
	s_and_b64 s[10:11], s[10:11], s[12:13]
	v_cndmask_b32_e64 v83, v83, v85, s[10:11]
	v_cndmask_b32_e64 v81, v81, 2, s[10:11]
	v_cmp_ne_u32_e64 s[10:11], 3, v80
	v_cmp_gt_f32_e64 s[12:13], v88, v83
	s_and_b64 s[10:11], s[10:11], s[12:13]
	v_cndmask_b32_e64 v83, v83, v88, s[10:11]
	v_cndmask_b32_e64 v81, v81, 3, s[10:11]
	v_cmp_ne_u32_e64 s[10:11], 4, v80
	v_cmp_gt_f32_e64 s[12:13], v89, v83
	s_and_b64 s[10:11], s[10:11], s[12:13]
	v_cndmask_b32_e64 v83, v83, v89, s[10:11]
	v_cndmask_b32_e64 v81, v81, 4, s[10:11]
	v_cmp_ne_u32_e64 s[10:11], 5, v80
	v_cmp_gt_f32_e64 s[12:13], v91, v83
	s_and_b64 s[10:11], s[10:11], s[12:13]
	v_cndmask_b32_e64 v83, v83, v91, s[10:11]
	v_cmp_gt_f32_e32 vcc, v93, v83
	v_cndmask_b32_e64 v81, v81, 5, s[10:11]
	s_and_b64 vcc, s[8:9], vcc
	v_cndmask_b32_e64 v81, v81, 6, vcc
	v_cndmask_b32_e32 v83, v83, v93, vcc
	s_and_saveexec_b64 s[8:9], s[6:7]
	s_cbranch_execz .LBB0_1373
	v_cmp_gt_f32_e32 vcc, v84, v83
	s_and_saveexec_b64 s[6:7], vcc
	s_cbranch_execz .LBB0_1372
	v_mov_b32_e32 v81, 7
	v_mov_b32_e32 v83, v84
	s_branch .LBB0_1372

; #define LAS __attribute__((address_space(3)))
; DI KArgP kargs() { KArgP p = (KArgP)__builtin_amdgcn_kernarg_segment_ptr(); asm volatile("" : "+s"(p)); return p; }
; #define PHASE_IDS() int tid = tidx(); asm volatile("" : "+v"(tid)); const int lane = tid & 63, wave = __builtin_amdgcn_readfirstlane(tid >> 6), gw = vcu * 8 + wave; (void)lane; (void)gw
; #define PHASE_WS() unsigned char* const ws = kargs()->ws
; template <bool ROUTE, bool COMBINE> ...
;     ...
;     const float rstd = 1.0f / sqrtf(wave_sum(s2) * (1.0f / D_) + LN_EPS);
;     float lg0 = 0.f, lg1 = 0.f, lg2 = 0.f, lg3 = 0.f, lg4 = 0.f, lg5 = 0.f, lg6 = 0.f, lg7 = 0.f;
; #pragma unroll
;     for (int j = 0; j < 4; ++j) {
;         const int c = 8 * lane + 512 * j;
;         const f32x4 oa = v[2 * j] * rstd * *(const f32x4*)(g + c) + *(const f32x4*)(bta + c), ob = v[2 * j + 1] * rstd * *(const f32x4*)(g + c + 4) + *(const f32x4*)(bta + c + 4);
; template <int l>
; DI void layer_body(LAS unsigned char* lds, const XcdBarrier& bar, const int lo, const int hi, const int G, const int vcu) {
;     ...
;         if (IN(pb + 8)) {
;             PHASE_WS();
;             PHASE_IDS();
;             const float* g2 = kargs()->in[19] + (size_t)l * D_; const float* b2 = kargs()->in[20] + (size_t)l * D_;
;             float* const xout_ = (l == DEPTH - 1) ? kargs()->out : (float*)nullptr;
;             bf16* const xb_ = (l == DEPTH - 1) ? (bf16*)nullptr : XB; unsigned char* const xb8_ = (l == DEPTH - 1) ? (unsigned char*)nullptr : (unsigned char*)(ws + WS_XB8);
;             if (!moe) { LN_PIPE((ln_row<false, false>(row, lane, Yb, g2, b2, xout_, xb_, xb8_, (const LAS float*)nullptr, nullptr, nullptr, nullptr, nullptr, nullptr, nullptr, cu_))); }
;             else { for (int row = gw; row < NTOK; row += NGW) ln_row<false, true>(row, lane, nullptr, g2, b2, xout_, xb_, xb8_, (const LAS float*)nullptr, nullptr, topg, X1B, YE2, pos, PLEB); }
.LBB0_1771:
	s_cmp_lt_i32 s78, 19
	s_cselect_b64 s[4:5], -1, 0
	s_and_b64 s[2:3], s[4:5], s[2:3]
	s_andn2_b64 vcc, exec, s[2:3]
	s_cbranch_vccnz .LBB0_1777
	s_mov_b64 s[8:9], s[0:1]
	s_getreg_b32 s2, hwreg(HW_REG_HW_ID, 0, 6)
	s_and_b32 s2, s2, 63
	s_lshl_b32 s2, s2, 2
	s_or_b32 s2, s2, 0x20c00
	v_mov_b32_e32 v0, s2
	ds_read_b32 v0, v0
	v_mbcnt_lo_u32_b32 v1, -1, 0
	v_mbcnt_hi_u32_b32 v1, -1, v1
	v_readlane_b32 s2, v254, 2
	s_lshl_b32 s2, s2, 3
	s_mov_b64 s[10:11], s[0:1]
	s_waitcnt lgkmcnt(0)
	v_readfirstlane_b32 s3, v0
	s_mov_b64 s[12:13], s[0:1]
	s_nop 0
	v_lshl_add_u32 v0, s3, 6, v1
	s_nop 0
	v_readfirstlane_b32 s3, v0
	s_ashr_i32 s14, s3, 6
	s_add_i32 s6, s14, s2
	s_cmpk_gt_i32 s6, 0x1fff
	s_cbranch_scc1 .LBB0_1777
	v_mbcnt_lo_u32_b32 v2, -1, 0
	v_mbcnt_hi_u32_b32 v2, -1, v2
	v_and_b32_e32 v3, 64, v2
	v_add_u32_e32 v3, 64, v3
	s_waitcnt vmcnt(22)
	v_xor_b32_e32 v5, 1, v2
	v_cmp_lt_i32_e32 vcc, v5, v3
	s_load_dwordx2 s[16:17], s[12:13], 0xa0
	s_load_dwordx2 s[2:3], s[8:9], 0xb0
	s_load_dwordx2 s[18:19], s[10:11], 0x98
	s_load_dwordx2 s[22:23], s[0:1], 0xa8
	v_cndmask_b32_e32 v5, v2, v5, vcc
	s_waitcnt vmcnt(13)
	v_lshlrev_b32_e32 v56, 2, v5
	v_xor_b32_e32 v5, 2, v2
	v_cmp_lt_i32_e32 vcc, v5, v3
	s_waitcnt lgkmcnt(0)
	s_add_u32 s0, s16, 0x2000
	s_addc_u32 s1, s17, 0
	v_cndmask_b32_e32 v5, v2, v5, vcc
	v_lshlrev_b32_e32 v57, 2, v5
	v_xor_b32_e32 v5, 4, v2
	v_cmp_lt_i32_e32 vcc, v5, v3
	s_add_u32 s8, s18, 0x2000
	v_lshlrev_b32_e32 v1, 3, v0
	v_cndmask_b32_e32 v5, v2, v5, vcc
	v_lshlrev_b32_e32 v58, 2, v5
	v_xor_b32_e32 v5, 8, v2
	v_cmp_lt_i32_e32 vcc, v5, v3
	s_addc_u32 s9, s19, 0
	s_add_u32 s15, s2, 0x18a10000
	v_cndmask_b32_e32 v5, v2, v5, vcc
	v_lshlrev_b32_e32 v59, 2, v5
	v_xor_b32_e32 v5, 16, v2
	v_cmp_lt_i32_e32 vcc, v5, v3
	v_and_b32_e32 v1, 0x1f8, v1
	s_addc_u32 s18, s3, 0
	v_cndmask_b32_e32 v5, v2, v5, vcc
	s_waitcnt vmcnt(12)
	v_lshlrev_b32_e32 v60, 2, v5
	v_xor_b32_e32 v5, 32, v2
	v_cmp_lt_i32_e32 vcc, v5, v3
	v_lshlrev_b32_e32 v4, 2, v1
	s_add_u32 s19, s2, 0x18a20000
	v_cndmask_b32_e32 v2, v2, v5, vcc
	v_mov_b32_e32 v5, 0
	v_lshlrev_b32_e32 v61, 2, v2
	v_or_b32_e32 v2, 0x800, v4
	v_mov_b32_e32 v3, v5
	s_addc_u32 s20, s3, 0
	v_lshl_add_u64 v[6:7], s[8:9], 0, v[4:5]
	v_lshl_add_u64 v[8:9], s[0:1], 0, v[4:5]
	v_lshl_add_u64 v[10:11], s[8:9], 0, v[2:3]
	v_lshl_add_u64 v[12:13], s[0:1], 0, v[2:3]
	v_or_b32_e32 v2, 0x1000, v4
	v_or_b32_e32 v4, 0x1800, v4
	s_cmp_lg_u64 s[22:23], 0
	v_lshl_add_u64 v[18:19], s[8:9], 0, v[4:5]
	v_lshl_add_u64 v[20:21], s[0:1], 0, v[4:5]
	v_lshlrev_b32_e32 v4, 1, v1
	s_cselect_b64 s[16:17], -1, 0
	v_lshl_add_u64 v[14:15], s[8:9], 0, v[2:3]
	v_lshl_add_u64 v[16:17], s[0:1], 0, v[2:3]
	v_lshl_add_u64 v[2:3], s[2:3], 0, v[4:5]
	s_mov_b64 s[0:1], 0x28700000
	s_ashr_i32 s7, s6, 31
	v_lshl_add_u64 v[22:23], v[2:3], 0, s[0:1]
	s_lshl_b64 s[0:1], s[6:7], 13
	v_and_b32_e32 v2, 63, v0
	s_add_u32 s0, s22, s0
	v_lshlrev_b32_e32 v4, 5, v2
	s_addc_u32 s1, s23, s1
	v_lshl_add_u64 v[0:1], s[0:1], 0, v[4:5]
	s_mov_b64 s[0:1], 0x1810
	v_lshl_add_u64 v[24:25], v[0:1], 0, s[0:1]
	v_readlane_b32 s0, v254, 2
	s_ashr_i32 s39, s38, 31
	s_lshl_b32 s0, s0, 4
	s_lshl_b32 s1, s14, 1
	s_lshl_b64 s[8:9], s[38:39], 13
	s_add_i32 s10, s0, s1
	s_lshl_b32 s21, s34, 4
	s_lshl_b64 s[0:1], s[6:7], 12
	s_add_u32 s0, s2, s0
	v_lshlrev_b32_e32 v4, 4, v2
	s_addc_u32 s1, s3, s1
	v_lshl_add_u64 v[0:1], s[0:1], 0, v[4:5]
	s_mov_b64 s[0:1], 0xca00c00
	v_lshl_add_u64 v[26:27], v[0:1], 0, s[0:1]
	v_cndmask_b32_e64 v0, 0, 1, s[16:17]
	s_lshl_b64 s[12:13], s[38:39], 12
	s_mov_b32 s7, 0xfa000000
	s_mov_b32 s14, 0x3fb504f3
	v_cmp_ne_u32_e64 s[0:1], 1, v0
	v_mov_b32_e32 v62, 0x3727c5ac
	s_mov_b32 s22, 0xf800000
	v_mov_b32_e32 v63, 0x260
	s_movk_i32 s23, 0xf000
	global_load_dwordx4 v[160:163], v[8:9], off offset:16
	global_load_dwordx4 v[164:167], v[6:7], off offset:16
	global_load_dwordx4 v[168:171], v[6:7], off
	global_load_dwordx4 v[172:175], v[8:9], off
	global_load_dwordx4 v[176:179], v[12:13], off offset:16
	global_load_dwordx4 v[180:183], v[10:11], off offset:16
	global_load_dwordx4 v[184:187], v[10:11], off
	global_load_dwordx4 v[188:191], v[12:13], off
	global_load_dwordx4 v[192:195], v[16:17], off offset:16
	global_load_dwordx4 v[196:199], v[14:15], off offset:16
	global_load_dwordx4 v[200:203], v[14:15], off
	global_load_dwordx4 v[204:207], v[16:17], off
	global_load_dwordx4 v[208:211], v[20:21], off offset:16
	global_load_dwordx4 v[212:215], v[18:19], off offset:16
	global_load_dwordx4 v[216:219], v[18:19], off
	global_load_dwordx4 v[220:223], v[20:21], off
	s_branch .LBB0_1775

; template <bool ROUTE, bool COMBINE> ...
;     ...
;         const int p0 = pos[row * 2], p1 = pos[row * 2 + 1]; const float g0 = topg[row * 2], g1 = topg[row * 2 + 1];
; #pragma unroll
;         for (int j = 0; j < 4; ++j) { const int c = 8 * lane + 512 * j;
;             f32x4 xa, xb, pa, pb, a0, a1, c0, c1;
;             bf8_to_f32(*(const u32x4*)(X1B + (size_t)row * D_ + c), xa, xb); bf8_to_f32(*(const u32x4*)(PLEB + (size_t)row * D_ + c), pa, pb);
;             bf8_to_f32(*(const u32x4*)(YE + (size_t)p0 * D_ + c), a0, a1);
;             bf8_to_f32(*(const u32x4*)(YE + (size_t)p1 * D_ + c), c0, c1);
;             v[2 * j] = (ALPHA * xa + (g0 * a0 + g1 * c0)) + pa; v[2 * j + 1] = (ALPHA * xb + (g0 * a1 + g1 * c1)) + pb; }
.LBB0_1775:
	s_ashr_i32 s11, s10, 31
	s_lshl_b64 s[2:3], s[10:11], 2
	s_add_u32 s16, s19, s2
	s_addc_u32 s17, s20, s3
	global_load_dwordx2 v[54:55], v5, s[16:17]
	global_load_dwordx4 v[0:3], v[26:27], off offset:-3072
	global_load_dwordx4 v[28:31], v[26:27], off offset:-2048
	global_load_dwordx4 v[32:35], v[26:27], off offset:-1024
	s_add_i32 s16, s10, 1
	s_ashr_i32 s17, s16, 31
	s_add_u32 s2, s15, s2
	s_waitcnt vmcnt(15)
	v_add_co_u32_e32 v84, vcc, s7, v26
	s_addc_u32 s3, s18, s3
	s_lshl_b64 s[16:17], s[16:17], 2
	v_addc_co_u32_e32 v85, vcc, -1, v27, vcc
	s_add_u32 s16, s15, s16
	global_load_dwordx4 v[36:39], v[84:85], off offset:-3072
	global_load_dwordx4 v[40:43], v[84:85], off offset:-2048
	global_load_dwordx4 v[46:49], v[84:85], off offset:-1024
	s_addc_u32 s17, s18, s17
	global_load_dword v4, v5, s[2:3]
	global_load_dword v44, v5, s[16:17]
	s_and_b64 vcc, exec, s[0:1]
	s_waitcnt vmcnt(8)
	v_ashrrev_i32_e32 v51, 31, v54
	v_mov_b32_e32 v50, v54
	v_ashrrev_i32_e32 v65, 31, v55
	s_waitcnt lgkmcnt(0)
	v_mov_b32_e32 v64, v55
	v_lshlrev_b64 v[50:51], 12, v[50:51]
	v_lshlrev_b64 v[54:55], 12, v[64:65]
	v_lshl_add_u64 v[92:93], v[22:23], 0, v[50:51]
	v_lshl_add_u64 v[54:55], v[22:23], 0, v[54:55]
	global_load_dwordx4 v[50:53], v[92:93], off
	global_load_dwordx4 v[64:67], v[54:55], off
	global_load_dwordx4 v[68:71], v[92:93], off offset:1024
	global_load_dwordx4 v[72:75], v[54:55], off offset:1024
	global_load_dwordx4 v[76:79], v[26:27], off
	global_load_dwordx4 v[80:83], v[84:85], off
	s_waitcnt vmcnt(13)
	v_lshlrev_b32_e32 v94, 16, v0
	v_and_b32_e32 v95, 0xffff0000, v0
	v_lshlrev_b32_e32 v96, 16, v1
	v_and_b32_e32 v97, 0xffff0000, v1
	global_load_dwordx4 v[84:87], v[92:93], off offset:2048
	v_lshlrev_b32_e32 v98, 16, v2
	v_and_b32_e32 v99, 0xffff0000, v2
	v_lshlrev_b32_e32 v100, 16, v3
	v_and_b32_e32 v101, 0xffff0000, v3
	global_load_dwordx4 v[0:3], v[54:55], off offset:2048
	s_waitcnt vmcnt(13)
	v_lshlrev_b32_e32 v106, 16, v32
	v_and_b32_e32 v107, 0xffff0000, v32
	v_lshlrev_b32_e32 v108, 16, v33
	v_and_b32_e32 v109, 0xffff0000, v33
	v_lshlrev_b32_e32 v110, 16, v34
	v_and_b32_e32 v111, 0xffff0000, v34
	v_lshlrev_b32_e32 v112, 16, v35
	v_and_b32_e32 v113, 0xffff0000, v35
	global_load_dwordx4 v[32:35], v[92:93], off offset:3072
	global_load_dwordx4 v[88:91], v[54:55], off offset:3072
	s_waitcnt vmcnt(12)
	v_lshlrev_b32_e32 v124, 16, v48
	v_and_b32_e32 v125, 0xffff0000, v48
	v_lshlrev_b32_e32 v126, 16, v49
	v_and_b32_e32 v127, 0xffff0000, v49
	v_lshlrev_b32_e32 v114, 16, v36
	v_and_b32_e32 v115, 0xffff0000, v36
	v_lshlrev_b32_e32 v36, 16, v37
	v_and_b32_e32 v37, 0xffff0000, v37
	v_lshlrev_b32_e32 v118, 16, v40
	v_and_b32_e32 v119, 0xffff0000, v40
	v_lshlrev_b32_e32 v40, 16, v41
	v_and_b32_e32 v41, 0xffff0000, v41
	v_lshlrev_b32_e32 v102, 16, v28
	v_and_b32_e32 v103, 0xffff0000, v28
	v_lshlrev_b32_e32 v28, 16, v29
	v_and_b32_e32 v29, 0xffff0000, v29
	v_lshlrev_b32_e32 v116, 16, v38
	v_and_b32_e32 v117, 0xffff0000, v38
	v_lshlrev_b32_e32 v38, 16, v39
	v_and_b32_e32 v39, 0xffff0000, v39
	v_lshlrev_b32_e32 v120, 16, v42
	v_and_b32_e32 v121, 0xffff0000, v42
	v_lshlrev_b32_e32 v42, 16, v43
	v_and_b32_e32 v43, 0xffff0000, v43
	v_lshlrev_b32_e32 v104, 16, v30
	v_and_b32_e32 v105, 0xffff0000, v30
	v_lshlrev_b32_e32 v30, 16, v31
	v_and_b32_e32 v31, 0xffff0000, v31
	v_lshlrev_b32_e32 v122, 16, v46
	v_and_b32_e32 v123, 0xffff0000, v46
	v_lshlrev_b32_e32 v46, 16, v47
	v_and_b32_e32 v47, 0xffff0000, v47
	s_waitcnt vmcnt(8)
	v_lshlrev_b32_e32 v92, 16, v64
	v_and_b32_e32 v93, 0xffff0000, v64
	v_lshlrev_b32_e32 v64, 16, v65
	v_and_b32_e32 v65, 0xffff0000, v65
	v_lshlrev_b32_e32 v128, 16, v66
	v_and_b32_e32 v129, 0xffff0000, v66
	v_lshlrev_b32_e32 v66, 16, v67
	v_and_b32_e32 v67, 0xffff0000, v67
	s_waitcnt vmcnt(6)
	v_lshlrev_b32_e32 v134, 16, v72
	v_and_b32_e32 v135, 0xffff0000, v72
	v_lshlrev_b32_e32 v72, 16, v73
	v_and_b32_e32 v73, 0xffff0000, v73
	v_lshlrev_b32_e32 v48, 16, v50
	v_and_b32_e32 v49, 0xffff0000, v50
	v_lshlrev_b32_e32 v50, 16, v51
	v_and_b32_e32 v51, 0xffff0000, v51
	v_lshlrev_b32_e32 v54, 16, v52
	v_and_b32_e32 v55, 0xffff0000, v52
	v_lshlrev_b32_e32 v52, 16, v53
	v_and_b32_e32 v53, 0xffff0000, v53
	v_lshlrev_b32_e32 v130, 16, v68
	v_and_b32_e32 v131, 0xffff0000, v68
	v_lshlrev_b32_e32 v68, 16, v69
	v_and_b32_e32 v69, 0xffff0000, v69
	v_lshlrev_b32_e32 v136, 16, v74
	v_and_b32_e32 v137, 0xffff0000, v74
	v_lshlrev_b32_e32 v74, 16, v75
	v_and_b32_e32 v75, 0xffff0000, v75
	s_waitcnt vmcnt(2)
; template <bool ROUTE, bool COMBINE> ...
;     ...
;         for (int j = 0; j < 4; ++j) { const int c = 8 * lane + 512 * j;
;             f32x4 xa, xb, pa, pb, a0, a1, c0, c1;
;             bf8_to_f32(*(const u32x4*)(X1B + (size_t)row * D_ + c), xa, xb); bf8_to_f32(*(const u32x4*)(PLEB + (size_t)row * D_ + c), pa, pb);
;             bf8_to_f32(*(const u32x4*)(YE + (size_t)p0 * D_ + c), a0, a1);
;             bf8_to_f32(*(const u32x4*)(YE + (size_t)p1 * D_ + c), c0, c1);
;             v[2 * j] = (ALPHA * xa + (g0 * a0 + g1 * c0)) + pa; v[2 * j + 1] = (ALPHA * xb + (g0 * a1 + g1 * c1)) + pb; }
;     }
; #pragma unroll
;     for (int j = 0; j < 8; ++j) s += (v[j].x + v[j].y) + (v[j].z + v[j].w);
	v_lshlrev_b32_e32 v144, 16, v2
	v_and_b32_e32 v145, 0xffff0000, v2
	v_lshlrev_b32_e32 v146, 16, v3
	v_and_b32_e32 v147, 0xffff0000, v3
	v_pk_mul_f32 v[2:3], v[44:45], v[92:93] op_sel_hi:[0,1]
	v_pk_mul_f32 v[64:65], v[44:45], v[64:65] op_sel_hi:[0,1]
	v_pk_mul_f32 v[92:93], v[44:45], v[128:129] op_sel_hi:[0,1]
	v_pk_mul_f32 v[66:67], v[44:45], v[66:67] op_sel_hi:[0,1]
	v_pk_mul_f32 v[72:73], v[44:45], v[72:73] op_sel_hi:[0,1]
	v_lshlrev_b32_e32 v132, 16, v70
	v_and_b32_e32 v133, 0xffff0000, v70
	v_lshlrev_b32_e32 v70, 16, v71
	v_and_b32_e32 v71, 0xffff0000, v71
	v_pk_mul_f32 v[74:75], v[44:45], v[74:75] op_sel_hi:[0,1]
	v_pk_fma_f32 v[50:51], v[4:5], v[50:51], v[64:65] op_sel_hi:[0,1,1]
	v_pk_fma_f32 v[2:3], v[4:5], v[48:49], v[2:3] op_sel_hi:[0,1,1]
	v_pk_fma_f32 v[48:49], v[4:5], v[52:53], v[66:67] op_sel_hi:[0,1,1]
	v_pk_fma_f32 v[52:53], v[4:5], v[54:55], v[92:93] op_sel_hi:[0,1,1]
	v_pk_fma_f32 v[54:55], v[4:5], v[68:69], v[72:73] op_sel_hi:[0,1,1]
	v_lshlrev_b32_e32 v142, 16, v0
	v_and_b32_e32 v143, 0xffff0000, v0
	v_lshlrev_b32_e32 v0, 16, v1
	v_and_b32_e32 v1, 0xffff0000, v1
	v_pk_fma_f32 v[66:67], v[4:5], v[70:71], v[74:75] op_sel_hi:[0,1,1]
	v_pk_fma_f32 v[36:37], v[36:37], s[14:15], v[50:51] op_sel_hi:[1,0,1]
	v_pk_fma_f32 v[40:41], v[40:41], s[14:15], v[54:55] op_sel_hi:[1,0,1]
	v_lshlrev_b32_e32 v138, 16, v84
	v_and_b32_e32 v139, 0xffff0000, v84
	v_lshlrev_b32_e32 v84, 16, v85
	v_and_b32_e32 v85, 0xffff0000, v85
	v_lshlrev_b32_e32 v140, 16, v86
	v_and_b32_e32 v141, 0xffff0000, v86
	v_pk_mul_f32 v[128:129], v[44:45], v[134:135] op_sel_hi:[0,1]
	v_pk_mul_f32 v[134:135], v[44:45], v[136:137] op_sel_hi:[0,1]
	v_pk_mul_f32 v[0:1], v[44:45], v[0:1] op_sel_hi:[0,1]
	v_pk_fma_f32 v[38:39], v[38:39], s[14:15], v[48:49] op_sel_hi:[1,0,1]
	v_pk_fma_f32 v[42:43], v[42:43], s[14:15], v[66:67] op_sel_hi:[1,0,1]
	v_pk_add_f32 v[48:49], v[36:37], v[96:97]
	v_pk_add_f32 v[36:37], v[40:41], v[28:29]
	v_pk_mul_f32 v[28:29], v[44:45], v[144:145] op_sel_hi:[0,1]
	v_lshlrev_b32_e32 v86, 16, v87
	v_and_b32_e32 v87, 0xffff0000, v87
	v_pk_fma_f32 v[64:65], v[4:5], v[130:131], v[128:129] op_sel_hi:[0,1,1]
	v_pk_fma_f32 v[68:69], v[4:5], v[132:133], v[134:135] op_sel_hi:[0,1,1]
	v_pk_add_f32 v[40:41], v[42:43], v[30:31]
	v_pk_fma_f32 v[0:1], v[4:5], v[84:85], v[0:1] op_sel_hi:[0,1,1]
	v_pk_mul_f32 v[30:31], v[44:45], v[146:147] op_sel_hi:[0,1]
	v_pk_fma_f32 v[28:29], v[4:5], v[140:141], v[28:29] op_sel_hi:[0,1,1]
	v_pk_fma_f32 v[64:65], v[118:119], s[14:15], v[64:65] op_sel_hi:[1,0,1]
	v_pk_fma_f32 v[68:69], v[120:121], s[14:15], v[68:69] op_sel_hi:[1,0,1]
	v_pk_fma_f32 v[0:1], v[46:47], s[14:15], v[0:1] op_sel_hi:[1,0,1]
	v_pk_fma_f32 v[30:31], v[4:5], v[86:87], v[30:31] op_sel_hi:[0,1,1]
	v_pk_fma_f32 v[46:47], v[124:125], s[14:15], v[28:29] op_sel_hi:[1,0,1]
	v_pk_fma_f32 v[70:71], v[116:117], s[14:15], v[52:53] op_sel_hi:[1,0,1]
	v_pk_add_f32 v[52:53], v[38:39], v[100:101]
	v_pk_add_f32 v[38:39], v[64:65], v[102:103]
	v_pk_add_f32 v[42:43], v[68:69], v[104:105]
	v_pk_fma_f32 v[28:29], v[126:127], s[14:15], v[30:31] op_sel_hi:[1,0,1]
	v_pk_add_f32 v[30:31], v[46:47], v[110:111]
	v_lshlrev_b32_e32 v46, 16, v80
	v_and_b32_e32 v47, 0xffff0000, v80
	v_lshlrev_b32_e32 v64, 16, v81
	v_and_b32_e32 v65, 0xffff0000, v81
	v_lshlrev_b32_e32 v66, 16, v82
	v_and_b32_e32 v67, 0xffff0000, v82
	v_lshlrev_b32_e32 v68, 16, v83
	v_and_b32_e32 v69, 0xffff0000, v83
	s_waitcnt vmcnt(1)
	v_lshlrev_b32_e32 v80, 16, v34
	v_and_b32_e32 v81, 0xffff0000, v34
	v_lshlrev_b32_e32 v82, 16, v35
	v_and_b32_e32 v83, 0xffff0000, v35
	s_waitcnt vmcnt(0)
	v_lshlrev_b32_e32 v34, 16, v88
	v_and_b32_e32 v35, 0xffff0000, v88
	v_pk_add_f32 v[54:55], v[70:71], v[98:99]
	v_lshlrev_b32_e32 v70, 16, v76
	v_and_b32_e32 v71, 0xffff0000, v76
	v_lshlrev_b32_e32 v72, 16, v77
	v_and_b32_e32 v73, 0xffff0000, v77
	v_lshlrev_b32_e32 v74, 16, v78
	v_and_b32_e32 v75, 0xffff0000, v78
	v_lshlrev_b32_e32 v76, 16, v79
	v_and_b32_e32 v77, 0xffff0000, v79
	v_lshlrev_b32_e32 v78, 16, v32
	v_and_b32_e32 v79, 0xffff0000, v32
	v_pk_mul_f32 v[34:35], v[44:45], v[34:35] op_sel_hi:[0,1]
	v_lshlrev_b32_e32 v84, 16, v89
	v_and_b32_e32 v85, 0xffff0000, v89
	v_lshlrev_b32_e32 v86, 16, v90
	v_and_b32_e32 v87, 0xffff0000, v90
	v_pk_fma_f32 v[34:35], v[4:5], v[78:79], v[34:35] op_sel_hi:[0,1,1]
	v_pk_fma_f32 v[2:3], v[114:115], s[14:15], v[2:3] op_sel_hi:[1,0,1]
	v_lshlrev_b32_e32 v32, 16, v33
	v_and_b32_e32 v33, 0xffff0000, v33
	v_lshlrev_b32_e32 v88, 16, v91
	v_and_b32_e32 v89, 0xffff0000, v91
	v_pk_mul_f32 v[84:85], v[44:45], v[84:85] op_sel_hi:[0,1]
	v_pk_fma_f32 v[34:35], v[46:47], s[14:15], v[34:35] op_sel_hi:[1,0,1]
	v_pk_mul_f32 v[46:47], v[44:45], v[86:87] op_sel_hi:[0,1]
	v_pk_mul_f32 v[136:137], v[44:45], v[142:143] op_sel_hi:[0,1]
	v_pk_add_f32 v[50:51], v[2:3], v[94:95]
	v_pk_fma_f32 v[32:33], v[4:5], v[32:33], v[84:85] op_sel_hi:[0,1,1]
	v_pk_mul_f32 v[44:45], v[44:45], v[88:89] op_sel_hi:[0,1]
	v_pk_fma_f32 v[46:47], v[4:5], v[80:81], v[46:47] op_sel_hi:[0,1,1]
	v_pk_fma_f32 v[32:33], v[64:65], s[14:15], v[32:33] op_sel_hi:[1,0,1]
	v_pk_fma_f32 v[44:45], v[4:5], v[82:83], v[44:45] op_sel_hi:[0,1,1]
	v_pk_fma_f32 v[46:47], v[66:67], s[14:15], v[46:47] op_sel_hi:[1,0,1]
	v_mov_b32_e32 v64, v54
	v_mov_b32_e32 v65, v50
	v_mov_b32_e32 v66, v55
	v_mov_b32_e32 v67, v51
	v_pk_fma_f32 v[44:45], v[68:69], s[14:15], v[44:45] op_sel_hi:[1,0,1]
	v_pk_add_f32 v[64:65], v[64:65], v[66:67]
	v_mov_b32_e32 v66, v52
	v_mov_b32_e32 v67, v48
	v_mov_b32_e32 v68, v53
	v_mov_b32_e32 v69, v49
	v_pk_add_f32 v[66:67], v[66:67], v[68:69]
	v_pk_fma_f32 v[2:3], v[4:5], v[138:139], v[136:137] op_sel_hi:[0,1,1]
	v_pk_add_f32 v[64:65], v[64:65], v[66:67]
; DI float wave_sum(float v) {
; #pragma unroll
;     for (int o = 1; o < 64; o <<= 1) v += __shfl_xor(v, o);
;     return v;
; template <bool ROUTE, bool COMBINE> ...
;     ...
;     for (int j = 0; j < 8; ++j) s += (v[j].x + v[j].y) + (v[j].z + v[j].w);
;     const float mean = wave_sum(s) * (1.0f / D_); float s2 = 0.f;
; #pragma unroll
;     for (int j = 0; j < 8; ++j) { v[j] = v[j] - mean; s2 += (v[j].x * v[j].x + v[j].y * v[j].y) + (v[j].z * v[j].z + v[j].w * v[j].w); }
;     const float rstd = 1.0f / sqrtf(wave_sum(s2) * (1.0f / D_) + LN_EPS);
	v_pk_mov_b32 v[66:67], v[38:39], v[36:37] op_sel:[1,0]
	v_mov_b32_e32 v68, v38
	v_mov_b32_e32 v69, v37
	v_pk_fma_f32 v[2:3], v[122:123], s[14:15], v[2:3] op_sel_hi:[1,0,1]
	v_pk_add_f32 v[66:67], v[66:67], v[68:69]
	v_pk_add_f32 v[0:1], v[0:1], v[108:109]
	v_pk_add_f32 v[2:3], v[2:3], v[106:107]
	v_add_f32_e32 v4, 0, v65
	v_pk_add_f32 v[66:67], v[66:67], v[66:67] op_sel:[0,1] op_sel_hi:[1,0]
	v_pk_add_f32 v[34:35], v[34:35], v[70:71]
	v_add_f32_e32 v64, v64, v4
	v_add_f32_e32 v68, v42, v43
	v_add_f32_e32 v70, v40, v41
	v_mov_b32_e32 v69, v2
	v_mov_b32_e32 v71, v3
	v_mov_b32_e32 v65, v0
	v_mov_b32_e32 v67, v1
	v_pk_add_f32 v[28:29], v[28:29], v[112:113]
	v_pk_add_f32 v[68:69], v[68:69], v[70:71]
	v_pk_add_f32 v[64:65], v[64:65], v[66:67]
	v_pk_mov_b32 v[66:67], v[30:31], v[28:29] op_sel:[1,0]
	v_pk_add_f32 v[64:65], v[68:69], v[64:65]
	v_mov_b32_e32 v68, v30
	v_mov_b32_e32 v69, v29
	v_pk_add_f32 v[66:67], v[66:67], v[68:69]
	v_pk_add_f32 v[32:33], v[32:33], v[72:73]
	v_pk_add_f32 v[44:45], v[44:45], v[76:77]
	v_pk_add_f32 v[46:47], v[46:47], v[74:75]
	v_pk_add_f32 v[64:65], v[64:65], v[64:65] op_sel_hi:[0,1]
	v_pk_add_f32 v[66:67], v[66:67], v[66:67] op_sel_hi:[0,1]
	v_add_f32_e32 v69, v34, v35
	v_add_f32_e32 v71, v32, v33
	v_mov_b32_e32 v66, v46
	v_mov_b32_e32 v64, v47
	v_mov_b32_e32 v68, v44
	v_mov_b32_e32 v70, v45
	v_pk_add_f32 v[64:65], v[66:67], v[64:65]
	v_pk_add_f32 v[66:67], v[68:69], v[70:71]
	s_nop 0
	v_pk_add_f32 v[64:65], v[64:65], v[66:67]
	s_nop 0
	v_add_f32_e32 v4, v64, v65
	ds_bpermute_b32 v64, v56, v4
	s_waitcnt lgkmcnt(0)
	v_add_f32_e32 v4, v4, v64
	ds_bpermute_b32 v64, v57, v4
	s_waitcnt lgkmcnt(0)
	v_add_f32_e32 v4, v4, v64
	ds_bpermute_b32 v64, v58, v4
	s_waitcnt lgkmcnt(0)
	v_add_f32_e32 v4, v4, v64
	ds_bpermute_b32 v64, v59, v4
	s_waitcnt lgkmcnt(0)
	v_add_f32_e32 v4, v4, v64
	ds_bpermute_b32 v64, v60, v4
	s_waitcnt lgkmcnt(0)
	v_add_f32_e32 v4, v4, v64
	ds_bpermute_b32 v64, v61, v4
	s_waitcnt lgkmcnt(0)
	v_add_f32_e32 v4, v4, v64
	v_fmamk_f32 v49, v4, 0xba000000, v49
	v_fmamk_f32 v51, v4, 0xba000000, v51
	v_fmac_f32_e32 v48, 0xba000000, v4
	v_fmac_f32_e32 v50, 0xba000000, v4
	v_mul_f32_e32 v64, v51, v51
	v_mul_f32_e32 v65, v49, v49
	v_fmac_f32_e32 v64, v50, v50
	v_fmac_f32_e32 v65, v48, v48
	v_fmamk_f32 v53, v4, 0xba000000, v53
	v_fmamk_f32 v55, v4, 0xba000000, v55
	v_add_f32_e32 v64, v64, v65
	v_fmac_f32_e32 v52, 0xba000000, v4
	v_fmac_f32_e32 v54, 0xba000000, v4
	v_mul_f32_e32 v65, v55, v55
	v_mul_f32_e32 v66, v53, v53
	v_fmac_f32_e32 v65, v54, v54
	v_fmac_f32_e32 v66, v52, v52
	v_add_f32_e32 v65, v65, v66
	v_fmamk_f32 v37, v4, 0xba000000, v37
	v_fmamk_f32 v39, v4, 0xba000000, v39
	v_add_f32_e32 v64, v64, v65
	v_fmac_f32_e32 v36, 0xba000000, v4
	v_fmac_f32_e32 v38, 0xba000000, v4
	v_mul_f32_e32 v65, v39, v39
	v_mul_f32_e32 v66, v37, v37
	v_fmac_f32_e32 v65, v38, v38
	v_fmac_f32_e32 v66, v36, v36
	v_add_f32_e32 v65, v65, v66
	v_fmamk_f32 v41, v4, 0xba000000, v41
	v_fmamk_f32 v43, v4, 0xba000000, v43
	v_add_f32_e32 v64, v65, v64
	v_fmac_f32_e32 v40, 0xba000000, v4
	v_fmac_f32_e32 v42, 0xba000000, v4
	v_mul_f32_e32 v65, v43, v43
	v_mul_f32_e32 v66, v41, v41
	v_fmac_f32_e32 v65, v42, v42
	v_fmac_f32_e32 v66, v40, v40
	v_add_f32_e32 v65, v65, v66
	v_fmamk_f32 v1, v4, 0xba000000, v1
	v_fmamk_f32 v3, v4, 0xba000000, v3
	v_add_f32_e32 v64, v65, v64
	v_fmac_f32_e32 v0, 0xba000000, v4
	v_fmac_f32_e32 v2, 0xba000000, v4
	v_mul_f32_e32 v65, v3, v3
	v_mul_f32_e32 v66, v1, v1
	v_fmac_f32_e32 v65, v2, v2
	v_fmac_f32_e32 v66, v0, v0
	v_add_f32_e32 v65, v65, v66
	v_fmamk_f32 v29, v4, 0xba000000, v29
	v_fmamk_f32 v31, v4, 0xba000000, v31
	v_add_f32_e32 v64, v65, v64
	v_fmac_f32_e32 v28, 0xba000000, v4
	v_fmac_f32_e32 v30, 0xba000000, v4
	v_mul_f32_e32 v65, v31, v31
	v_mul_f32_e32 v66, v29, v29
	v_fmac_f32_e32 v65, v30, v30
	v_fmac_f32_e32 v66, v28, v28
	v_add_f32_e32 v65, v65, v66
	v_fmamk_f32 v33, v4, 0xba000000, v33
	v_fmamk_f32 v35, v4, 0xba000000, v35
	v_add_f32_e32 v64, v65, v64
	v_fmac_f32_e32 v32, 0xba000000, v4
	v_fmac_f32_e32 v34, 0xba000000, v4
	v_mul_f32_e32 v65, v35, v35
	v_mul_f32_e32 v66, v33, v33
	v_fmac_f32_e32 v65, v34, v34
	v_fmac_f32_e32 v66, v32, v32
	v_add_f32_e32 v65, v65, v66
	v_fmamk_f32 v45, v4, 0xba000000, v45
	v_fmamk_f32 v47, v4, 0xba000000, v47
	v_add_f32_e32 v64, v65, v64
	v_fmac_f32_e32 v44, 0xba000000, v4
	v_fmac_f32_e32 v46, 0xba000000, v4
	v_mul_f32_e32 v4, v47, v47
	v_mul_f32_e32 v65, v45, v45
	v_fmac_f32_e32 v4, v46, v46
	v_fmac_f32_e32 v65, v44, v44
	v_add_f32_e32 v4, v4, v65
	v_add_f32_e32 v4, v4, v64
	ds_bpermute_b32 v64, v56, v4
	s_waitcnt lgkmcnt(0)
	v_add_f32_e32 v4, v4, v64
	ds_bpermute_b32 v64, v57, v4
	s_waitcnt lgkmcnt(0)
	v_add_f32_e32 v4, v4, v64
	ds_bpermute_b32 v64, v58, v4
	s_waitcnt lgkmcnt(0)
	v_add_f32_e32 v4, v4, v64
	ds_bpermute_b32 v64, v59, v4
	s_waitcnt lgkmcnt(0)
	v_add_f32_e32 v4, v4, v64
	ds_bpermute_b32 v64, v60, v4
	s_waitcnt lgkmcnt(0)
	v_add_f32_e32 v4, v4, v64
	ds_bpermute_b32 v64, v61, v4
	s_cbranch_vccnz .LBB0_1774
; template <bool ROUTE, bool COMBINE> ...
;     ...
;     const float rstd = 1.0f / sqrtf(wave_sum(s2) * (1.0f / D_) + LN_EPS);
;     float lg0 = 0.f, lg1 = 0.f, lg2 = 0.f, lg3 = 0.f, lg4 = 0.f, lg5 = 0.f, lg6 = 0.f, lg7 = 0.f;
; #pragma unroll
;     for (int j = 0; j < 4; ++j) {
;         const int c = 8 * lane + 512 * j;
;         const f32x4 oa = v[2 * j] * rstd * *(const f32x4*)(g + c) + *(const f32x4*)(bta + c), ob = v[2 * j + 1] * rstd * *(const f32x4*)(g + c + 4) + *(const f32x4*)(bta + c + 4);
;         if (X) { *(f32x4*)(X + (size_t)row * D_ + c) = oa; *(f32x4*)(X + (size_t)row * D_ + c + 4) = ob; }
	s_waitcnt lgkmcnt(0)
	v_add_f32_e32 v4, v4, v64
	v_fmamk_f32 v4, v4, 0x3a000000, v62
	v_mul_f32_e32 v64, 0x4f800000, v4
	v_cmp_gt_f32_e32 vcc, s22, v4
	s_nop 1
	v_cndmask_b32_e32 v4, v4, v64, vcc
	v_sqrt_f32_e32 v64, v4
	s_nop 0
	v_add_u32_e32 v65, -1, v64
	v_add_u32_e32 v82, 1, v64
	v_fma_f32 v83, -v65, v64, v4
	v_fma_f32 v84, -v82, v64, v4
	v_cmp_ge_f32_e64 s[2:3], 0, v83
	s_nop 1
	v_cndmask_b32_e64 v64, v64, v65, s[2:3]
	v_cmp_lt_f32_e64 s[2:3], 0, v84
	s_nop 1
	v_cndmask_b32_e64 v64, v64, v82, s[2:3]
	v_mul_f32_e32 v65, 0x37800000, v64
	v_cndmask_b32_e32 v64, v64, v65, vcc
	v_cmp_class_f32_e32 vcc, v4, v63
	s_nop 1
	v_cndmask_b32_e32 v4, v64, v4, vcc
	v_div_scale_f32 v64, s[2:3], v4, v4, 1.0
	v_rcp_f32_e32 v65, v64
	v_add_co_u32_e32 v82, vcc, s23, v24
	v_fma_f32 v85, -v64, v65, 1.0
	s_nop 0
	v_addc_co_u32_e32 v83, vcc, -1, v25, vcc
	v_div_scale_f32 v84, vcc, 1.0, v4, 1.0
	v_fmac_f32_e32 v65, v85, v65
	v_mul_f32_e32 v85, v84, v65
	v_fma_f32 v86, -v64, v85, v84
	v_fmac_f32_e32 v85, v86, v65
	v_fma_f32 v64, -v64, v85, v84
	v_div_fmas_f32 v64, v64, v65, v85
	v_div_fixup_f32 v4, v64, v4, 1.0
	v_pk_mul_f32 v[54:55], v[54:55], v[4:5] op_sel_hi:[1,0]
	v_pk_mul_f32 v[52:53], v[52:53], v[4:5] op_sel_hi:[1,0]
	v_pk_mul_f32 v[64:65], v[50:51], v[4:5] op_sel_hi:[1,0]
	v_pk_mul_f32 v[84:85], v[48:49], v[4:5] op_sel_hi:[1,0]
	v_pk_mul_f32 v[42:43], v[42:43], v[4:5] op_sel_hi:[1,0]
	v_pk_mul_f32 v[40:41], v[40:41], v[4:5] op_sel_hi:[1,0]
	v_pk_mul_f32 v[30:31], v[30:31], v[4:5] op_sel_hi:[1,0]
	v_pk_mul_f32 v[28:29], v[28:29], v[4:5] op_sel_hi:[1,0]
	v_pk_mul_f32 v[46:47], v[46:47], v[4:5] op_sel_hi:[1,0]
	v_pk_mul_f32 v[44:45], v[44:45], v[4:5] op_sel_hi:[1,0]
	v_pk_mul_f32 v[34:35], v[34:35], v[4:5] op_sel_hi:[1,0]
	v_pk_mul_f32 v[32:33], v[32:33], v[4:5] op_sel_hi:[1,0]
	v_pk_fma_f32 v[50:51], v[52:53], v[166:167], v[162:163]
	v_pk_fma_f32 v[48:49], v[54:55], v[164:165], v[160:161]
	v_pk_fma_f32 v[54:55], v[84:85], v[170:171], v[174:175]
	v_pk_fma_f32 v[52:53], v[64:65], v[168:169], v[172:173]
	global_store_dwordx4 v[82:83], v[52:55], off offset:-2064
	global_store_dwordx4 v[82:83], v[48:51], off offset:-2048
	s_nop 1
	v_pk_mul_f32 v[72:73], v[38:39], v[4:5] op_sel_hi:[1,0]
	v_pk_mul_f32 v[74:75], v[36:37], v[4:5] op_sel_hi:[1,0]
	v_pk_fma_f32 v[38:39], v[40:41], v[182:183], v[178:179]
	v_pk_fma_f32 v[36:37], v[42:43], v[180:181], v[176:177]
	v_pk_fma_f32 v[42:43], v[74:75], v[186:187], v[190:191]
	v_pk_fma_f32 v[40:41], v[72:73], v[184:185], v[188:189]
	global_store_dwordx4 v[82:83], v[40:43], off offset:-16
	global_store_dwordx4 v[24:25], v[36:39], off offset:-4096
	s_nop 1
	v_pk_mul_f32 v[64:65], v[2:3], v[4:5] op_sel_hi:[1,0]
	v_pk_mul_f32 v[66:67], v[0:1], v[4:5] op_sel_hi:[1,0]
	v_pk_fma_f32 v[2:3], v[28:29], v[198:199], v[194:195]
	v_pk_fma_f32 v[0:1], v[30:31], v[196:197], v[192:193]
	v_pk_fma_f32 v[30:31], v[66:67], v[202:203], v[206:207]
	v_pk_fma_f32 v[28:29], v[64:65], v[200:201], v[204:205]
	global_store_dwordx4 v[24:25], v[28:31], off offset:-2064
	global_store_dwordx4 v[24:25], v[0:3], off offset:-2048
	s_nop 1
	v_pk_fma_f32 v[2:3], v[44:45], v[214:215], v[210:211]
	v_pk_fma_f32 v[0:1], v[46:47], v[212:213], v[208:209]
	v_pk_fma_f32 v[30:31], v[32:33], v[218:219], v[222:223]
	v_pk_fma_f32 v[28:29], v[34:35], v[216:217], v[220:221]
	global_store_dwordx4 v[24:25], v[28:31], off offset:-16
	global_store_dwordx4 v[24:25], v[0:3], off
	s_nop 1
	s_branch .LBB0_1774
